# dead lane-index ops removed after DPP conversion (on v10)
# speedup vs baseline: 1.0054x; 1.0017x over previous
; __device__ __forceinline__ int opaque_tid() { int t = threadIdx.x; asm volatile("" : "+v"(t)); return t; }
; __device__ __forceinline__ unsigned char* opaque_ptr(unsigned char* q) { long z = 0; asm volatile("" : "+s"(z)); return q + z; }
; __device__ __forceinline__ void ph_norm1_tables(const Params& p) {
;     const int tid = opaque_tid(), lane = tid & 63, wave = tid >> 6;
;     unsigned char* ws = opaque_ptr(p.ws);
;     const float* mod = (const float*)(ws + WS_MOD);
;     for (int it = blockIdx.x; it < N1_ROWITEMS; it += gridDim.x) {
;         {
;             const int row = it * 8 + wave; const int rr = row < NLAT ? (row >> 11) : 4;
;             const float* xr = row < NLAT ? p.in[I_X] + (size_t)row * DM : p.in[I_CTX] + (size_t)(row - NLAT) * DM;
;             f32x4 x[8], y[8];
; #pragma unroll
;             for (int j = 0; j < 8; ++j) x[j] = *(const f32x4*)(xr + j * 256 + lane * 4);
;             const float* m = mod + (size_t)rr * 12288;
;             rms_mod_store(x, p.in[I_N1G], m + DM, m, (bf16_t*)(ws + WS_H) + (size_t)row * DM, y, lane);
.LBB0_144:
	s_cmp_lt_i32 s86, 2
	s_cselect_b64 s[2:3], -1, 0
	s_and_b64 s[0:1], s[2:3], s[0:1]
	s_andn2_b64 vcc, exec, s[0:1]
	s_cbranch_vccnz .LBB0_152
	s_cmpk_gt_i32 s92, 0x47f
	v_mov_b32_e32 v1, v0
	s_mov_b64 s[0:1], 0
	s_cbranch_scc1 .LBB0_152
	v_ashrrev_i32_e32 v3, 6, v1
	v_lshlrev_b32_e32 v1, 2, v1
	v_and_b32_e32 v2, 0xfc, v1
	v_mbcnt_lo_u32_b32 v1, -1, 0
	v_mbcnt_hi_u32_b32 v4, -1, v1
	v_and_b32_e32 v1, 64, v4
	v_add_u32_e32 v5, 64, v1
	v_readlane_b32 s8, v251, 0
	v_mov_b32_e32 v39, 0
	v_or_b32_e32 v10, 0x400, v2
	v_lshlrev_b32_e32 v38, 2, v2
	v_readlane_b32 s16, v251, 8
	v_readlane_b32 s17, v251, 9
	v_or_b32_e32 v12, 0x500, v2
	v_lshl_add_u64 v[40:41], s[16:17], 0, v[38:39]
	v_lshlrev_b32_e32 v38, 2, v10
	v_or_b32_e32 v14, 0x600, v2
	v_lshl_add_u64 v[42:43], s[16:17], 0, v[38:39]
	v_lshlrev_b32_e32 v38, 2, v12
	s_add_u32 s4, s84, s0
	v_xor_b32_e32 v6, 1, v4
	v_or_b32_e32 v16, 0x700, v2
	v_lshl_add_u64 v[44:45], s[16:17], 0, v[38:39]
	v_lshlrev_b32_e32 v38, 2, v14
	s_addc_u32 s5, s85, s1
	v_cmp_lt_i32_e32 vcc, v6, v5
	v_lshl_add_u64 v[46:47], s[16:17], 0, v[38:39]
	v_lshlrev_b32_e32 v38, 2, v16
	s_add_u32 s0, s4, 0x10000
	v_lshl_add_u64 v[48:49], s[16:17], 0, v[38:39]
	v_lshlrev_b32_e32 v38, 1, v2
	s_addc_u32 s1, s5, 0
	v_or_b32_e32 v4, 0x100, v2
	v_or_b32_e32 v6, 0x200, v2
	v_or_b32_e32 v8, 0x300, v2
	v_readlane_b32 s9, v251, 1
	v_readlane_b32 s10, v251, 2
	v_readlane_b32 s11, v251, 3
	v_readlane_b32 s12, v251, 4
	v_lshl_add_u64 v[18:19], s[4:5], 0, v[38:39]
	s_mov_b64 s[4:5], 0x1cdb8000
	v_lshl_add_u64 v[50:51], v[18:19], 0, s[4:5]
	v_lshl_add_u32 v52, s92, 3, v3
	s_lshl_b32 s8, s94, 3
	s_movk_i32 s9, 0x1fff
	v_lshlrev_b32_e32 v54, 2, v2
	s_movk_i32 s10, 0x1000
	s_mov_b64 s[4:5], 0x2000
	v_mov_b32_e32 v73, 0x358637bd
	s_mov_b32 s11, 0x800000
	v_lshlrev_b32_e32 v56, 2, v4
	v_lshlrev_b32_e32 v38, 2, v6
	v_lshlrev_b32_e32 v58, 2, v8
	v_lshlrev_b32_e32 v60, 2, v10
	v_lshlrev_b32_e32 v62, 2, v12
	v_lshlrev_b32_e32 v64, 2, v14
	v_lshlrev_b32_e32 v66, 2, v16
	v_mov_b32_e32 v55, v39
	v_mov_b32_e32 v57, v39
	s_mov_b32 s12, s92
	v_readlane_b32 s13, v251, 5
	v_readlane_b32 s14, v251, 6
	v_readlane_b32 s15, v251, 7
	v_readlane_b32 s18, v251, 10
	v_readlane_b32 s19, v251, 11
	v_readlane_b32 s20, v251, 12
	v_readlane_b32 s21, v251, 13
	v_readlane_b32 s22, v251, 14
	v_readlane_b32 s23, v251, 15
	s_branch .LBB0_148

; #define LAS __attribute__((address_space(3)))
; __device__ __forceinline__ unsigned cvt_pk_bf16(float lo, float hi) { const f32x2 v = {lo, hi}; const bf16x2_t b = __builtin_convertvector(v, bf16x2_t); return __builtin_bit_cast(unsigned, b); }
; __device__ __forceinline__ int opaque_tid() { int t = threadIdx.x; asm volatile("" : "+v"(t)); return t; }
; __device__ __forceinline__ unsigned char* opaque_ptr(unsigned char* q) { long z = 0; asm volatile("" : "+s"(z)); return q + z; }
; __device__ __forceinline__ void sgu_unit(const Params& p, int l, int un, LAS unsigned char* lds) {
;     const int tid = opaque_tid(), lane = tid & 63, wave = tid >> 6;
;     unsigned char* ws = opaque_ptr(p.ws);
;     const bf16_t* P = (const bf16_t*)(ws + WS_PA);
;     bf16_t* CAT = (bf16_t*)(ws + WS_CAT);
;     const int cc = un >> 2, h = un & 3; const int row0 = cc * 128;
;     LAS bf16_t* Wl = (LAS bf16_t*)lds;
;     LAS bf16_t* Vl = (LAS bf16_t*)(lds + 128 * 136 * 2);
;     const float* Wg = p.in[I_SGUW] + ((size_t)l * 4 + h) * 128 * 128;
;     f32x4 wq[8]; u32x4 vv[16];
; #pragma unroll
;     for (int i = 0; i < 8; ++i) wq[i] = *(const f32x4*)(Wg + (i * 512 + tid) * 4);
; #pragma unroll
;     for (int qi = 0; qi < 16; ++qi) vv[qi] = *(const u32x4*)(P + (size_t)(row0 + wave * 16 + qi) * INP + C_SGU_V + lane * 8);
; #pragma unroll
;     for (int i = 0; i < 8; ++i) { const int e4 = (i * 512 + tid) * 4, r = e4 >> 7, c = e4 & 127; const f32x4 v = wq[i];
;         u32x2 w; w.x = cvt_pk_bf16(v[0], v[1]); w.y = cvt_pk_bf16(v[2], v[3]); *(LAS u32x2*)(Wl + r * 136 + c) = w; }
.LBB0_474:
	s_and_b64 vcc, exec, s[2:3]
	s_cbranch_vccz .LBB0_539
	s_cmpk_gt_i32 s31, 0x47f
	s_cbranch_scc0 .LBB0_511
	s_cmpk_gt_u32 s31, 0x59f
	s_cbranch_scc1 .LBB0_510
	v_mov_b32_e32 v64, v0
	s_mov_b64 s[0:1], 0
	s_add_u32 s42, s84, s0
	s_addc_u32 s43, s85, s1
	s_add_u32 s14, s42, 0x1f1b8000
	s_addc_u32 s15, s43, 0
	s_and_b32 s0, s31, 3
	v_readlane_b32 s44, v251, 16
	s_lshl_b32 s19, s0, 7
	v_readlane_b32 s45, v251, 17
	v_readlane_b32 s46, v251, 18
	v_readlane_b32 s47, v251, 19
	v_readlane_b32 s48, v251, 20
	v_readlane_b32 s49, v251, 21
	v_readlane_b32 s50, v251, 22
	v_readlane_b32 s51, v251, 23
	s_lshl_b32 s1, s31, 5
	s_or_b32 s4, s19, s18
	v_readlane_b32 s52, v251, 24
	v_readlane_b32 s53, v251, 25
	v_readlane_b32 s54, v251, 26
	v_readlane_b32 s55, v251, 27
	s_mov_b64 s[44:45], s[48:49]
	s_add_i32 s1, s1, 0x7fff7000
	s_lshl_b64 s[2:3], s[4:5], 9
	s_mov_b64 s[46:47], s[50:51]
	s_add_u32 s2, s46, s2
	v_lshlrev_b32_e32 v2, 2, v64
	s_addc_u32 s3, s47, s3
	v_ashrrev_i32_e32 v3, 31, v2
	v_add_u32_e32 v62, 0x800, v2
	v_lshl_add_u64 v[4:5], v[2:3], 2, s[2:3]
	v_ashrrev_i32_e32 v63, 31, v62
	v_lshl_add_u64 v[6:7], v[62:63], 2, s[2:3]
	global_load_dwordx4 v[66:69], v[4:5], off
	global_load_dwordx4 v[70:73], v[6:7], off
	v_add_u32_e32 v126, 0x1000, v2
	v_ashrrev_i32_e32 v127, 31, v126
	v_add_u32_e32 v128, 0x1800, v2
	v_lshl_add_u64 v[4:5], v[126:127], 2, s[2:3]
	v_ashrrev_i32_e32 v129, 31, v128
	v_lshl_add_u64 v[6:7], v[128:129], 2, s[2:3]
	global_load_dwordx4 v[98:101], v[4:5], off
	global_load_dwordx4 v[102:105], v[6:7], off
	v_add_u32_e32 v130, 0x2000, v2
	v_ashrrev_i32_e32 v131, 31, v130
	v_add_u32_e32 v132, 0x2800, v2
	v_lshl_add_u64 v[4:5], v[130:131], 2, s[2:3]
	v_ashrrev_i32_e32 v133, 31, v132
	v_lshl_add_u64 v[6:7], v[132:133], 2, s[2:3]
	global_load_dwordx4 v[106:109], v[4:5], off
	global_load_dwordx4 v[110:113], v[6:7], off
	v_add_u32_e32 v134, 0x3000, v2
	v_add_u32_e32 v136, 0x3800, v2
	v_ashrrev_i32_e32 v135, 31, v134
	v_ashrrev_i32_e32 v137, 31, v136
	v_ashrrev_i32_e32 v127, 6, v64
	v_lshl_add_u64 v[4:5], v[134:135], 2, s[2:3]
	v_lshl_add_u64 v[2:3], v[136:137], 2, s[2:3]
	s_and_b32 s60, s1, 0x7fffff80
	v_lshlrev_b32_e32 v65, 4, v127
	v_and_b32_e32 v8, 63, v64
	global_load_dwordx4 v[114:117], v[4:5], off
	global_load_dwordx4 v[118:121], v[2:3], off
	v_add_u32_e32 v9, s60, v65
	v_mov_b64_e32 v[2:3], s[14:15]
	s_movk_i32 s1, 0x1e00
	v_mad_i64_i32 v[4:5], s[2:3], v9, s1, v[2:3]
	v_lshlrev_b32_e32 v206, 4, v8
	v_or_b32_e32 v6, 1, v9
	v_lshl_add_u64 v[4:5], v[4:5], 0, v[206:207]
	v_mad_i64_i32 v[6:7], s[2:3], v6, s1, v[2:3]
	v_lshl_add_u64 v[6:7], v[6:7], 0, v[206:207]
	global_load_dwordx4 v[122:125], v[4:5], off offset:1024
	global_load_dwordx4 v[58:61], v[6:7], off offset:1024
	v_or_b32_e32 v4, 2, v9
	v_or_b32_e32 v6, 3, v9
	v_mad_i64_i32 v[4:5], s[2:3], v4, s1, v[2:3]
	v_mad_i64_i32 v[6:7], s[2:3], v6, s1, v[2:3]
	v_lshl_add_u64 v[4:5], v[4:5], 0, v[206:207]
	v_lshl_add_u64 v[6:7], v[6:7], 0, v[206:207]
	global_load_dwordx4 v[54:57], v[4:5], off offset:1024
	global_load_dwordx4 v[50:53], v[6:7], off offset:1024
	v_or_b32_e32 v4, 4, v9
	v_or_b32_e32 v6, 5, v9
	v_mad_i64_i32 v[4:5], s[2:3], v4, s1, v[2:3]
	v_mad_i64_i32 v[6:7], s[2:3], v6, s1, v[2:3]
	v_lshl_add_u64 v[4:5], v[4:5], 0, v[206:207]
	v_lshl_add_u64 v[6:7], v[6:7], 0, v[206:207]
	global_load_dwordx4 v[46:49], v[4:5], off offset:1024
	global_load_dwordx4 v[42:45], v[6:7], off offset:1024
	v_or_b32_e32 v4, 6, v9
	v_or_b32_e32 v6, 7, v9
	v_mad_i64_i32 v[4:5], s[2:3], v4, s1, v[2:3]
	v_mad_i64_i32 v[6:7], s[2:3], v6, s1, v[2:3]
	v_lshl_add_u64 v[4:5], v[4:5], 0, v[206:207]
	v_lshl_add_u64 v[6:7], v[6:7], 0, v[206:207]
	global_load_dwordx4 v[38:41], v[4:5], off offset:1024
	global_load_dwordx4 v[34:37], v[6:7], off offset:1024
	v_or_b32_e32 v4, 8, v9
	v_or_b32_e32 v6, 9, v9
	v_mad_i64_i32 v[4:5], s[2:3], v4, s1, v[2:3]
	v_mad_i64_i32 v[6:7], s[2:3], v6, s1, v[2:3]
	v_lshl_add_u64 v[4:5], v[4:5], 0, v[206:207]
	v_lshl_add_u64 v[6:7], v[6:7], 0, v[206:207]
	global_load_dwordx4 v[30:33], v[4:5], off offset:1024
	global_load_dwordx4 v[26:29], v[6:7], off offset:1024
	v_or_b32_e32 v4, 10, v9
	v_or_b32_e32 v6, 11, v9
	v_mad_i64_i32 v[4:5], s[2:3], v4, s1, v[2:3]
	v_mad_i64_i32 v[6:7], s[2:3], v6, s1, v[2:3]
	v_lshl_add_u64 v[4:5], v[4:5], 0, v[206:207]
	v_lshl_add_u64 v[6:7], v[6:7], 0, v[206:207]
	global_load_dwordx4 v[22:25], v[4:5], off offset:1024
	global_load_dwordx4 v[18:21], v[6:7], off offset:1024
	v_or_b32_e32 v4, 12, v9
	v_or_b32_e32 v6, 13, v9
	v_mad_i64_i32 v[4:5], s[2:3], v4, s1, v[2:3]
	v_mad_i64_i32 v[6:7], s[2:3], v6, s1, v[2:3]
	v_lshl_add_u64 v[4:5], v[4:5], 0, v[206:207]
	v_lshl_add_u64 v[6:7], v[6:7], 0, v[206:207]
	v_lshlrev_b32_e32 v129, 3, v64
	global_load_dwordx4 v[14:17], v[4:5], off offset:1024
	global_load_dwordx4 v[10:13], v[6:7], off offset:1024
	v_or_b32_e32 v4, 14, v9
	v_or_b32_e32 v6, 15, v9
	v_and_b32_e32 v63, 0xf8, v129
	v_mad_i64_i32 v[4:5], s[2:3], v4, s1, v[2:3]
	v_mad_i64_i32 v[2:3], s[2:3], v6, s1, v[2:3]
	v_add_u32_e32 v138, 0, v63
	v_bfe_i32 v63, v64, 5, 25
	s_movk_i32 s44, 0x110
	v_lshl_add_u64 v[4:5], v[4:5], 0, v[206:207]
	v_lshl_add_u64 v[2:3], v[2:3], 0, v[206:207]
	s_waitcnt vmcnt(21)
	v_cvt_pk_bf16_f32 v66, v66, v67
	v_cvt_pk_bf16_f32 v67, v68, v69
	v_mad_u64_u32 v[68:69], s[2:3], v63, s44, v[138:139]
	global_load_dwordx4 v[6:9], v[4:5], off offset:1024
	s_nop 0
	global_load_dwordx4 v[2:5], v[2:3], off offset:1024
	ds_write_b64 v68, v[66:67]
	v_ashrrev_i32_e32 v66, 7, v62
	s_waitcnt vmcnt(22)
	v_cvt_pk_bf16_f32 v62, v70, v71
	v_cvt_pk_bf16_f32 v63, v72, v73
	v_mad_u64_u32 v[66:67], s[2:3], v66, s44, v[138:139]
	ds_write_b64 v66, v[62:63]
	v_ashrrev_i32_e32 v66, 7, v126
	s_waitcnt vmcnt(21)
; __device__ __forceinline__ float bflo(unsigned w) { return __uint_as_float(w << 16); }
; __device__ __forceinline__ float bfhi(unsigned w) { return __uint_as_float(w & 0xffff0000u); }
; __device__ __forceinline__ unsigned short f2bf(float f) { return (unsigned short)(cvt_pk_bf16(f, 0.f) & 0xffffu); }
; __device__ __forceinline__ float wave_sum(float v) {
; #pragma unroll
;     for (int o = 32; o >= 1; o >>= 1) v += __shfl_xor(v, o);
;     return v;
; __device__ __forceinline__ void sgu_unit(const Params& p, int l, int un, LAS unsigned char* lds) {
;     ...
;     for (int qi = 0; qi < 16; ++qi) { const int q = wave * 16 + qi;
;         const u32x4 v = vv[qi]; float f[8] = {bflo(v.x), bfhi(v.x), bflo(v.y), bfhi(v.y), bflo(v.z), bfhi(v.z), bflo(v.w), bfhi(v.w)}; float ss = 0.f;
; #pragma unroll
;         for (int j = 0; j < 8; ++j) { f[j] = gelu_tanh(f[j]); ss += f[j] * f[j]; }
;         ss = wave_sum(ss); const float rinv = rsqrtf(ss * (1.0f / 512.0f) + EPS);
;         if ((lane >> 4) == h) { const int c0 = (lane & 15) * 8; const float* g = p.in[I_SGUNG] + l * 512 + h * 128 + c0;
; #pragma unroll
;             for (int j = 0; j < 8; ++j) Vl[(c0 + j) * 136 + q] = f2bf(f[j] * rinv * g[j]); } }
	v_cvt_pk_bf16_f32 v62, v98, v99
	v_cvt_pk_bf16_f32 v63, v100, v101
	v_mad_u64_u32 v[66:67], s[2:3], v66, s44, v[138:139]
	ds_write_b64 v66, v[62:63]
	v_ashrrev_i32_e32 v66, 7, v128
	s_waitcnt vmcnt(20)
	v_cvt_pk_bf16_f32 v62, v102, v103
	v_cvt_pk_bf16_f32 v63, v104, v105
	v_mad_u64_u32 v[66:67], s[2:3], v66, s44, v[138:139]
	ds_write_b64 v66, v[62:63]
	v_ashrrev_i32_e32 v66, 7, v130
	s_waitcnt vmcnt(19)
	v_cvt_pk_bf16_f32 v62, v106, v107
	v_cvt_pk_bf16_f32 v63, v108, v109
	v_mad_u64_u32 v[66:67], s[2:3], v66, s44, v[138:139]
	ds_write_b64 v66, v[62:63]
	v_ashrrev_i32_e32 v66, 7, v132
	s_waitcnt vmcnt(18)
	v_cvt_pk_bf16_f32 v62, v110, v111
	v_cvt_pk_bf16_f32 v63, v112, v113
	v_mad_u64_u32 v[66:67], s[2:3], v66, s44, v[138:139]
	ds_write_b64 v66, v[62:63]
	v_ashrrev_i32_e32 v66, 7, v134
	s_waitcnt vmcnt(17)
	v_cvt_pk_bf16_f32 v62, v114, v115
	v_cvt_pk_bf16_f32 v63, v116, v117
	v_mad_u64_u32 v[66:67], s[2:3], v66, s44, v[138:139]
	ds_write_b64 v66, v[62:63]
	v_ashrrev_i32_e32 v66, 7, v136
	v_mad_u64_u32 v[66:67], s[2:3], v66, s44, v[138:139]
	s_waitcnt vmcnt(15)
	v_and_b32_e32 v67, 0xffff0000, v122
	v_mul_f32_e32 v77, 0x3dd2d3e8, v67
	v_fma_f32 v77, -v77, v67, s33
	v_mul_f32_e32 v77, v77, v67
	v_exp_f32_e32 v77, v77
	v_cvt_pk_bf16_f32 v62, v118, v119
	v_cvt_pk_bf16_f32 v63, v120, v121
	ds_write_b64 v66, v[62:63]
	v_lshlrev_b32_e32 v66, 16, v122
	v_add_f32_e32 v77, 1.0, v77
	v_mul_f32_e32 v73, 0x3dd2d3e8, v66
	v_rcp_f32_e32 v77, v77
	v_fma_f32 v73, -v73, v66, s33
	v_mul_f32_e32 v73, v73, v66
	v_lshlrev_b32_e32 v70, 16, v123
	v_exp_f32_e32 v73, v73
	v_mul_f32_e32 v102, v77, v67
	v_mul_f32_e32 v67, 0x3dd2d3e8, v70
	v_fma_f32 v67, -v67, v70, s33
	v_mul_f32_e32 v67, v67, v70
	v_add_f32_e32 v73, 1.0, v73
	v_exp_f32_e32 v67, v67
	v_rcp_f32_e32 v73, v73
	v_lshlrev_b32_e32 v72, 16, v124
	v_and_b32_e32 v71, 0xffff0000, v123
	v_add_f32_e32 v67, 1.0, v67
	v_mul_f32_e32 v77, 0x3dd2d3e8, v72
	v_mul_f32_e32 v104, v73, v66
	v_mul_f32_e32 v73, 0x3dd2d3e8, v71
	v_rcp_f32_e32 v67, v67
	v_fma_f32 v77, -v77, v72, s33
	v_fma_f32 v73, -v73, v71, s33
	v_mul_f32_e32 v77, v77, v72
	v_mul_f32_e32 v73, v73, v71
	v_exp_f32_e32 v77, v77
	v_and_b32_e32 v98, 0xffff0000, v124
	v_exp_f32_e32 v73, v73
	v_mul_f32_e32 v103, v67, v70
	v_mul_f32_e32 v70, 0x3dd2d3e8, v98
	v_fma_f32 v70, -v70, v98, s33
	v_add_f32_e32 v67, 1.0, v77
	v_mul_f32_e32 v70, v70, v98
	v_add_f32_e32 v73, 1.0, v73
	v_rcp_f32_e32 v67, v67
	v_exp_f32_e32 v70, v70
	v_rcp_f32_e32 v73, v73
	v_lshlrev_b32_e32 v105, 16, v125
	v_and_b32_e32 v106, 0xffff0000, v125
	v_mul_f32_e32 v99, v67, v72
	v_add_f32_e32 v67, 1.0, v70
	v_mul_f32_e32 v70, 0x3dd2d3e8, v105
	v_mul_f32_e32 v101, v73, v71
	v_fma_f32 v70, -v70, v105, s33
	v_mul_f32_e32 v71, 0x3dd2d3e8, v106
	v_mul_f32_e32 v70, v70, v105
	v_fma_f32 v71, -v71, v106, s33
	v_rcp_f32_e32 v67, v67
	v_exp_f32_e32 v70, v70
	v_mul_f32_e32 v71, v71, v106
	v_exp_f32_e32 v71, v71
	v_mul_f32_e32 v66, v102, v102
	v_mul_f32_e32 v100, v67, v98
	v_add_f32_e32 v67, 1.0, v70
	v_fmac_f32_e32 v66, v104, v104
	v_rcp_f32_e32 v67, v67
	v_add_f32_e32 v70, 1.0, v71
	v_fmac_f32_e32 v66, v103, v103
	v_rcp_f32_e32 v70, v70
	v_and_b32_e32 v62, 64, v249
	v_fmac_f32_e32 v66, v101, v101
	v_add_u32_e32 v62, 64, v62
	v_xor_b32_e32 v63, 32, v249
	v_fmac_f32_e32 v66, v99, v99
	v_cmp_lt_i32_e32 vcc, v63, v62
	v_fmac_f32_e32 v66, v100, v100
	v_mul_f32_e32 v98, v67, v105
	v_cndmask_b32_e32 v63, v249, v63, vcc
	v_fmac_f32_e32 v66, v98, v98
	v_mul_f32_e32 v77, v70, v106
	v_lshlrev_b32_e32 v68, 2, v63
	v_fmac_f32_e32 v66, v77, v77
	v_mov_b32_e32 v67, v66
	s_nop 1
	v_permlane32_swap_b32_e32 v67, v66
	v_lshl_add_u32 v107, v127, 5, 0
	v_readlane_b32 s56, v251, 28
	s_waitcnt lgkmcnt(0)
	v_add_f32_e32 v66, v66, v67
	v_mov_b32_e32 v67, v66
	s_nop 1
	v_permlane16_swap_b32_e32 v67, v66
	v_xor_b32_e32 v63, 8, v249
	v_cmp_lt_i32_e32 vcc, v63, v62
	v_readlane_b32 s57, v251, 29
	v_readlane_b32 s58, v251, 30
	v_cndmask_b32_e32 v63, v249, v63, vcc
	v_lshlrev_b32_e32 v70, 2, v63
	s_waitcnt lgkmcnt(0)
	v_add_f32_e32 v66, v66, v67
	s_nop 1
	v_mov_b32_dpp v67, v66 row_ror:8 row_mask:0xf bank_mask:0xf
	v_readlane_b32 s59, v251, 31
	s_mov_b64 s[48:49], s[52:53]
	s_waitcnt lgkmcnt(0)
	v_add_f32_e32 v67, v66, v67
	s_nop 1
	v_mov_b32_dpp v105, v67 row_shl:4 row_mask:0xf bank_mask:0x5
	v_mov_b32_dpp v105, v67 row_shr:4 row_mask:0xf bank_mask:0xa
	v_bfe_u32 v66, v64, 4, 2
	v_xor_b32_e32 v63, 1, v249
	s_mov_b64 s[50:51], s[54:55]
	s_nop 0
	s_waitcnt lgkmcnt(0)
	v_add_f32_e32 v62, v67, v105
	s_nop 1
	v_mov_b32_dpp v63, v62 quad_perm:[2,3,0,1] row_mask:0xf bank_mask:0xf
	v_cmp_eq_u32_e32 vcc, s0, v66
	s_lshl_b32 s0, s0, 9
	v_and_b32_e32 v67, 0x78, v129
	s_add_u32 s0, s25, s0
	s_waitcnt lgkmcnt(0)
	v_add_f32_e32 v105, v62, v63
	s_nop 1
	v_mov_b32_dpp v106, v105 quad_perm:[1,0,3,2] row_mask:0xf bank_mask:0xf
	s_addc_u32 s1, s26, 0
	v_lshlrev_b32_e32 v206, 2, v67
	v_lshl_add_u64 v[62:63], s[0:1], 0, v[206:207]
	v_mad_u32_u24 v67, v67, s44, v107
	s_and_saveexec_b64 s[0:1], vcc
	s_cbranch_execz .LBB0_479
	s_waitcnt lgkmcnt(0)
	v_add_f32_e32 v105, v105, v106
	v_fmamk_f32 v105, v105, 0x3b000000, v246
	s_mov_b32 s2, 0x800000
	v_cmp_gt_f32_e64 s[2:3], s2, v105
	v_mul_f32_e32 v106, 0x4b800000, v105
	s_nop 0
	v_cndmask_b32_e64 v105, v105, v106, s[2:3]
	v_rsq_f32_e32 v105, v105
	s_nop 0
	v_mul_f32_e32 v106, 0x45800000, v105
	v_cndmask_b32_e64 v112, v105, v106, s[2:3]
	v_mul_f32_e32 v113, v104, v112
	global_load_dwordx4 v[104:107], v[62:63], off offset:16
	global_load_dwordx4 v[108:111], v[62:63], off
	v_mul_f32_e32 v102, v102, v112
	v_mul_f32_e32 v99, v99, v112
	v_mul_f32_e32 v101, v101, v112
	v_mul_f32_e32 v98, v98, v112
	v_mul_f32_e32 v77, v77, v112
	s_waitcnt vmcnt(1)
	v_mul_f32_e32 v99, v99, v104
	s_waitcnt vmcnt(0)
	v_mov_b32_e32 v160, v108
	v_mov_b32_e32 v161, v109
	v_mov_b32_e32 v162, v110
	v_mov_b32_e32 v163, v111
	v_mov_b32_e32 v164, v104
	v_mov_b32_e32 v165, v105
	v_mov_b32_e32 v166, v106
	v_mov_b32_e32 v167, v107
	v_mul_f32_e32 v102, v102, v109
	v_cvt_pk_bf16_f32 v102, v102, s0
	v_cvt_pk_bf16_f32 v99, v99, s0
	ds_write_b16 v67, v102 offset:35088
	v_mul_f32_e32 v102, v103, v112
	ds_write_b16 v67, v99 offset:35904
	v_mul_f32_e32 v99, v100, v112
	v_mul_f32_e32 v108, v113, v108
	v_mul_f32_e32 v102, v102, v110
	v_mul_f32_e32 v101, v101, v111
	v_mul_f32_e32 v99, v99, v105
	v_mul_f32_e32 v98, v98, v106
	v_mul_f32_e32 v77, v77, v107
	v_cvt_pk_bf16_f32 v108, v108, s0
	v_cvt_pk_bf16_f32 v102, v102, s0
	v_cvt_pk_bf16_f32 v101, v101, s0
	v_cvt_pk_bf16_f32 v99, v99, s0
	v_cvt_pk_bf16_f32 v98, v98, s0
	v_cvt_pk_bf16_f32 v77, v77, s0
	ds_write_b16 v67, v108 offset:34816
	ds_write_b16 v67, v102 offset:35360
	ds_write_b16 v67, v101 offset:35632
	ds_write_b16 v67, v99 offset:36176
	ds_write_b16 v67, v98 offset:36448
	ds_write_b16 v67, v77 offset:36720

; __device__ __forceinline__ unsigned cvt_pk_bf16(float lo, float hi) { const f32x2 v = {lo, hi}; const bf16x2_t b = __builtin_convertvector(v, bf16x2_t); return __builtin_bit_cast(unsigned, b); }
; __device__ __forceinline__ float bflo(unsigned w) { return __uint_as_float(w << 16); }
; __device__ __forceinline__ float bfhi(unsigned w) { return __uint_as_float(w & 0xffff0000u); }
; template <bool MAIN, bool CONV>
; __device__ __forceinline__ void b_row(const Params& p, unsigned char* ws, int l, int row, int lane) {
;     ...
;         { float f[8]; float ss = 0.f;
;           if (lane < 48) { const u32x4 v = vq; f[0] = bflo(v.x); f[1] = bfhi(v.x); f[2] = bflo(v.y); f[3] = bfhi(v.y); f[4] = bflo(v.z); f[5] = bfhi(v.z); f[6] = bflo(v.w); f[7] = bfhi(v.w);
;     #pragma unroll
;               for (int j = 0; j < 8; ++j) ss += f[j] * f[j]; }
;           else {
;     #pragma unroll
;               for (int j = 0; j < 8; ++j) f[j] = 0.f; }
;           ss = wave_sum(ss); const float rinv = rsqrtf(ss * (1.0f / 384.0f) + EPS);
;           if (lane < 48) { u32x4 w;
;               w.x = cvt_pk_bf16(f[0] * rinv * gq0[0], f[1] * rinv * gq0[1]); w.y = cvt_pk_bf16(f[2] * rinv * gq0[2], f[3] * rinv * gq0[3]);
;               w.z = cvt_pk_bf16(f[4] * rinv * gq1[0], f[5] * rinv * gq1[1]); w.w = cvt_pk_bf16(f[6] * rinv * gq1[2], f[7] * rinv * gq1[3]);
;               *(u32x4*)((bf16_t*)(ws + WS_QA) + (size_t)row * 384 + lane * 8) = w; } }
.LBB0_525:
	s_or_b64 exec, exec, s[0:1]
	s_waitcnt vmcnt(13)
	v_and_b32_e32 v70, 64, v249
	v_add_u32_e32 v117, 64, v70
	v_mov_b32_e32 v70, v116
	s_nop 1
	v_permlane32_swap_b32_e32 v70, v116
	s_waitcnt lgkmcnt(0)
	v_add_f32_e32 v72, v116, v70
	v_xor_b32_e32 v70, 16, v249
	v_cmp_lt_i32_e32 vcc, v70, v117
	s_nop 1
	v_cndmask_b32_e32 v70, v249, v70, vcc
	v_lshlrev_b32_e32 v70, 2, v70
	v_mov_b32_e32 v73, v72
	s_nop 1
	v_permlane16_swap_b32_e32 v73, v72
	s_waitcnt lgkmcnt(0)
	v_add_f32_e32 v73, v72, v73
	s_nop 1
	v_mov_b32_dpp v116, v73 row_ror:8 row_mask:0xf bank_mask:0xf
	s_waitcnt lgkmcnt(0)
	v_add_f32_e32 v116, v73, v116
	s_nop 1
	v_mov_b32_dpp v118, v116 row_shl:4 row_mask:0xf bank_mask:0x5
	v_mov_b32_dpp v118, v116 row_shr:4 row_mask:0xf bank_mask:0xa
	s_waitcnt lgkmcnt(0)
	v_add_f32_e32 v118, v116, v118
	s_nop 1
	v_mov_b32_dpp v119, v118 quad_perm:[2,3,0,1] row_mask:0xf bank_mask:0xf
	s_waitcnt lgkmcnt(0)
	v_add_f32_e32 v118, v118, v119
	v_xor_b32_e32 v119, 1, v249
	v_cmp_lt_i32_e32 vcc, v119, v117
	s_nop 1
	s_nop 1
	v_mov_b32_dpp v119, v118 quad_perm:[1,0,3,2] row_mask:0xf bank_mask:0xf
	s_and_saveexec_b64 s[0:1], s[36:37]
	s_cbranch_execz .LBB0_527
	s_waitcnt lgkmcnt(0)
	v_add_f32_e32 v118, v118, v119
	v_fmamk_f32 v118, v118, 0x3b2aaaab, v246
	s_mov_b32 s2, 0x800000
	v_mul_f32_e32 v119, 0x4b800000, v118
	v_cmp_gt_f32_e32 vcc, s2, v118
	s_movk_i32 s2, 0x300
	s_nop 0
	v_cndmask_b32_e32 v118, v118, v119, vcc
	v_rsq_f32_e32 v118, v118
	s_nop 0
	v_mul_f32_e32 v119, 0x45800000, v118
	v_cndmask_b32_e32 v118, v118, v119, vcc
	v_pk_mul_f32 v[106:107], v[106:107], v[118:119] op_sel_hi:[1,0]
	v_pk_mul_f32 v[108:109], v[108:109], v[118:119] op_sel_hi:[1,0]
	s_waitcnt vmcnt(10)
	v_pk_mul_f32 v[66:67], v[66:67], v[106:107]
	v_pk_mul_f32 v[68:69], v[68:69], v[108:109]
	v_cvt_pk_bf16_f32 v66, v66, v67
	v_cvt_pk_bf16_f32 v67, v68, v69
	v_pk_mul_f32 v[68:69], v[110:111], v[118:119] op_sel_hi:[1,0]
	s_nop 0
	v_pk_mul_f32 v[58:59], v[58:59], v[68:69]
	s_nop 0
	v_cvt_pk_bf16_f32 v68, v58, v59
	v_pk_mul_f32 v[58:59], v[112:113], v[118:119] op_sel_hi:[1,0]
	s_nop 0
	v_pk_mul_f32 v[58:59], v[60:61], v[58:59]
	s_nop 0
	v_cvt_pk_bf16_f32 v69, v58, v59
	v_mad_i64_i32 v[58:59], s[2:3], v98, s2, v[90:91]
	global_store_dwordx4 v[58:59], v[66:69], off

; #define LAS __attribute__((address_space(3)))
; __device__ __forceinline__ int opaque_tid() { int t = threadIdx.x; asm volatile("" : "+v"(t)); return t; }
; __device__ __forceinline__ unsigned char* opaque_ptr(unsigned char* q) { long z = 0; asm volatile("" : "+s"(z)); return q + z; }
;     __device__ __forceinline__ void init(const void* A_, const void* B_, int G_, int c_) { T.init(A_, B_, DM, DM, NLAT / 256, INP / 256, 1, 0, 0, G_, c_, 0); }
; __device__ __forceinline__ void sgu_unit(const Params& p, int l, int un, LAS unsigned char* lds) {
;     const int tid = opaque_tid(), lane = tid & 63, wave = tid >> 6;
;     unsigned char* ws = opaque_ptr(p.ws);
;     const bf16_t* P = (const bf16_t*)(ws + WS_PA);
;     bf16_t* CAT = (bf16_t*)(ws + WS_CAT);
;     const int cc = un >> 2, h = un & 3; const int row0 = cc * 128;
;     LAS bf16_t* Wl = (LAS bf16_t*)lds;
;     LAS bf16_t* Vl = (LAS bf16_t*)(lds + 128 * 136 * 2);
;     const float* Wg = p.in[I_SGUW] + ((size_t)l * 4 + h) * 128 * 128;
;     f32x4 wq[8]; u32x4 vv[16];
; #pragma unroll
;     for (int i = 0; i < 8; ++i) wq[i] = *(const f32x4*)(Wg + (i * 512 + tid) * 4);
; #pragma unroll
;     for (int qi = 0; qi < 16; ++qi) vv[qi] = *(const u32x4*)(P + (size_t)(row0 + wave * 16 + qi) * INP + C_SGU_V + lane * 8);
; __global__ void __launch_bounds__(512, 2) fwd(Params p) {
;     ...
;             { pg8::TileSched S; S.init(ws + WS_UPK, (bf16_t*)(ws + WS_G2B) + (size_t)l * 32 * 256 * 512, 512, 512, 3, 1, 32, (size_t)768 * 512 * 2, (size_t)256 * 512 * 2, G, c, (l == 0 && G == 256) ? 32 : 0);
;               pg8::EpiS2 E{(bf16_t*)(ws + WS_GB)};
;               pg8::Unit u0; if (S.next(0, u0)) { carry_wait(p, l); pg8::gemm_phase(lds, pg8::Desc{512, 512, 512}, S, E); }
;               else if (G == 256) { const int un = c - (l == 0 ? 128 : 96); if (un >= 0) sgu_unit(p, l, un, lds); } }
.LBB0_1258:
	v_readlane_b32 s0, v251, 50
	v_readlane_b32 s2, v252, 20
	v_readlane_b32 s1, v251, 51
	v_readlane_b32 s3, v252, 21
	s_and_b64 s[0:1], s[0:1], s[2:3]
	s_and_b64 s[0:1], s[0:1], exec
	s_cselect_b32 s0, 32, 0
	v_readlane_b32 s2, v255, 11
	s_mul_hi_u32 s1, s0, s2
	v_readlane_b32 s3, v255, 12
	s_mul_i32 s1, s1, s3
	s_sub_i32 s0, s0, s1
	s_sub_i32 s1, s0, s3
	s_cmp_ge_u32 s0, s3
	s_cselect_b32 s0, s1, s0
	s_sub_i32 s1, s0, s3
	s_cmp_ge_u32 s0, s3
	s_cselect_b32 s0, s1, s0
	v_readlane_b32 s1, v255, 42
	s_sub_i32 s0, s1, s0
	s_ashr_i32 s1, s0, 31
	s_abs_i32 s0, s0
	s_mul_hi_u32 s2, s0, s2
	s_mul_i32 s2, s2, s3
	s_sub_i32 s0, s0, s2
	s_sub_i32 s2, s0, s3
	s_cmp_ge_u32 s0, s3
	s_cselect_b32 s0, s2, s0
	s_sub_i32 s2, s0, s3
	s_cmp_ge_u32 s0, s3
	s_cselect_b32 s0, s2, s0
	s_xor_b32 s0, s0, s1
	s_sub_i32 s26, s0, s1
	s_cmpk_gt_i32 s26, 0x5f
	s_mov_b64 s[0:1], -1
	s_barrier
	s_cbranch_scc0 .LBB0_1294
	v_readlane_b32 s0, v252, 20
	v_readlane_b32 s1, v252, 21
	s_and_b64 s[0:1], s[0:1], exec
	s_movk_i32 s0, 0xff80
	s_cselect_b32 s0, s0, 0xffffffa0
	s_add_i32 s0, s0, s92
	v_readlane_b32 s12, v251, 50
	s_cmp_lt_i32 s0, 0
	v_readlane_b32 s13, v251, 51
	s_cselect_b64 s[2:3], -1, 0
	s_xor_b64 s[12:13], s[12:13], -1
	s_or_b64 s[2:3], s[2:3], s[12:13]
	s_and_b64 vcc, exec, s[2:3]
	s_cbranch_vccnz .LBB0_1293
	v_readlane_b32 s2, v252, 5
	v_readlane_b32 s44, v251, 16
	s_lshl_b32 s1, s0, 5
	s_lshl_b32 s0, s2, 9
	v_readlane_b32 s2, v253, 39
	v_readlane_b32 s48, v251, 20
	v_readlane_b32 s49, v251, 21
	v_readlane_b32 s3, v252, 6
	s_or_b32 s40, s0, s2
	s_mov_b32 s41, s5
	v_readlane_b32 s50, v251, 22
	v_readlane_b32 s51, v251, 23
	v_readlane_b32 s52, v251, 24
	v_readlane_b32 s53, v251, 25
	v_readlane_b32 s54, v251, 26
	v_readlane_b32 s55, v251, 27
	s_mov_b64 s[12:13], s[48:49]
	s_lshl_b64 s[2:3], s[40:41], 9
	s_mov_b64 s[14:15], s[50:51]
	v_mov_b32_e32 v64, v0
	s_add_u32 s2, s14, s2
	s_addc_u32 s3, s15, s3
	v_lshlrev_b32_e32 v2, 2, v64
	v_ashrrev_i32_e32 v3, 31, v2
	v_add_u32_e32 v62, 0x800, v2
	s_mov_b64 s[14:15], 0
	v_lshl_add_u64 v[4:5], v[2:3], 2, s[2:3]
	v_ashrrev_i32_e32 v63, 31, v62
	v_lshl_add_u64 v[6:7], v[62:63], 2, s[2:3]
	global_load_dwordx4 v[66:69], v[4:5], off
	global_load_dwordx4 v[70:73], v[6:7], off
	v_add_u32_e32 v102, 0x1000, v2
	v_ashrrev_i32_e32 v103, 31, v102
	v_add_u32_e32 v104, 0x1800, v2
	v_lshl_add_u64 v[4:5], v[102:103], 2, s[2:3]
	v_ashrrev_i32_e32 v105, 31, v104
	s_and_b32 s12, s1, 0x7fffff80
	s_mov_b32 s1, s5
	v_lshl_add_u64 v[6:7], v[104:105], 2, s[2:3]
	global_load_dwordx4 v[74:77], v[4:5], off
	global_load_dwordx4 v[78:81], v[6:7], off
	s_lshl_b64 s[0:1], s[0:1], 2
	v_readlane_b32 s13, v253, 41
	v_add_u32_e32 v106, 0x2000, v2
	s_add_u32 s0, s13, s0
	v_readlane_b32 s13, v253, 42
	v_ashrrev_i32_e32 v107, 31, v106
	v_add_u32_e32 v108, 0x2800, v2
	s_addc_u32 s1, s13, s1
	v_lshl_add_u64 v[4:5], v[106:107], 2, s[2:3]
	v_ashrrev_i32_e32 v109, 31, v108
	s_add_u32 s36, s84, s14
	v_lshl_add_u64 v[6:7], v[108:109], 2, s[2:3]
	global_load_dwordx4 v[82:85], v[4:5], off
	global_load_dwordx4 v[86:89], v[6:7], off
	s_addc_u32 s37, s85, s15
	v_add_u32_e32 v110, 0x3000, v2
	v_add_u32_e32 v112, 0x3800, v2
	s_add_u32 s38, s36, 0x1f1b8000
	v_ashrrev_i32_e32 v111, 31, v110
	v_ashrrev_i32_e32 v113, 31, v112
	v_ashrrev_i32_e32 v103, 6, v64
	s_addc_u32 s39, s37, 0
	v_lshl_add_u64 v[4:5], v[110:111], 2, s[2:3]
	v_lshl_add_u64 v[2:3], v[112:113], 2, s[2:3]
	v_lshlrev_b32_e32 v65, 4, v103
	v_and_b32_e32 v8, 63, v64
	global_load_dwordx4 v[90:93], v[4:5], off
	global_load_dwordx4 v[94:97], v[2:3], off
	v_add_u32_e32 v9, s12, v65
	v_mov_b64_e32 v[2:3], s[38:39]
	s_movk_i32 s13, 0x1e00
	v_mad_i64_i32 v[4:5], s[2:3], v9, s13, v[2:3]
	v_lshlrev_b32_e32 v206, 4, v8
	v_or_b32_e32 v6, 1, v9
	v_lshl_add_u64 v[4:5], v[4:5], 0, v[206:207]
	v_mad_i64_i32 v[6:7], s[2:3], v6, s13, v[2:3]
	v_lshl_add_u64 v[6:7], v[6:7], 0, v[206:207]
	global_load_dwordx4 v[98:101], v[4:5], off offset:1024
	global_load_dwordx4 v[58:61], v[6:7], off offset:1024
	v_or_b32_e32 v4, 2, v9
	v_or_b32_e32 v6, 3, v9
	v_mad_i64_i32 v[4:5], s[2:3], v4, s13, v[2:3]
	v_mad_i64_i32 v[6:7], s[2:3], v6, s13, v[2:3]
	v_lshl_add_u64 v[4:5], v[4:5], 0, v[206:207]
	v_lshl_add_u64 v[6:7], v[6:7], 0, v[206:207]
	global_load_dwordx4 v[54:57], v[4:5], off offset:1024
	global_load_dwordx4 v[50:53], v[6:7], off offset:1024
	v_or_b32_e32 v4, 4, v9
	v_or_b32_e32 v6, 5, v9
	v_mad_i64_i32 v[4:5], s[2:3], v4, s13, v[2:3]
	v_mad_i64_i32 v[6:7], s[2:3], v6, s13, v[2:3]
	v_lshl_add_u64 v[4:5], v[4:5], 0, v[206:207]
	v_lshl_add_u64 v[6:7], v[6:7], 0, v[206:207]
	global_load_dwordx4 v[46:49], v[4:5], off offset:1024
	global_load_dwordx4 v[42:45], v[6:7], off offset:1024
	v_or_b32_e32 v4, 6, v9
	v_or_b32_e32 v6, 7, v9
	v_mad_i64_i32 v[4:5], s[2:3], v4, s13, v[2:3]
	v_mad_i64_i32 v[6:7], s[2:3], v6, s13, v[2:3]
	v_lshl_add_u64 v[4:5], v[4:5], 0, v[206:207]
	v_lshl_add_u64 v[6:7], v[6:7], 0, v[206:207]
	global_load_dwordx4 v[38:41], v[4:5], off offset:1024
	global_load_dwordx4 v[34:37], v[6:7], off offset:1024
	v_or_b32_e32 v4, 8, v9
	v_or_b32_e32 v6, 9, v9
	v_mad_i64_i32 v[4:5], s[2:3], v4, s13, v[2:3]
	v_mad_i64_i32 v[6:7], s[2:3], v6, s13, v[2:3]
	v_lshl_add_u64 v[4:5], v[4:5], 0, v[206:207]
	v_lshl_add_u64 v[6:7], v[6:7], 0, v[206:207]
	global_load_dwordx4 v[30:33], v[4:5], off offset:1024
	global_load_dwordx4 v[26:29], v[6:7], off offset:1024
	v_or_b32_e32 v4, 10, v9
	v_or_b32_e32 v6, 11, v9
	v_mad_i64_i32 v[4:5], s[2:3], v4, s13, v[2:3]
	v_mad_i64_i32 v[6:7], s[2:3], v6, s13, v[2:3]
	v_lshl_add_u64 v[4:5], v[4:5], 0, v[206:207]
	v_lshl_add_u64 v[6:7], v[6:7], 0, v[206:207]
	global_load_dwordx4 v[22:25], v[4:5], off offset:1024
	global_load_dwordx4 v[18:21], v[6:7], off offset:1024
	v_or_b32_e32 v4, 12, v9
	v_or_b32_e32 v6, 13, v9
	v_mad_i64_i32 v[4:5], s[2:3], v4, s13, v[2:3]
	v_mad_i64_i32 v[6:7], s[2:3], v6, s13, v[2:3]
	v_lshl_add_u64 v[4:5], v[4:5], 0, v[206:207]
	v_lshl_add_u64 v[6:7], v[6:7], 0, v[206:207]
	v_lshlrev_b32_e32 v105, 3, v64
	global_load_dwordx4 v[14:17], v[4:5], off offset:1024
	global_load_dwordx4 v[10:13], v[6:7], off offset:1024
	v_or_b32_e32 v4, 14, v9
	v_or_b32_e32 v6, 15, v9
	v_and_b32_e32 v63, 0xf8, v105
	v_mad_i64_i32 v[4:5], s[2:3], v4, s13, v[2:3]
	v_mad_i64_i32 v[2:3], s[2:3], v6, s13, v[2:3]
	v_add_u32_e32 v114, 0, v63
	v_bfe_i32 v63, v64, 5, 25
	s_movk_i32 s13, 0x110
	v_lshl_add_u64 v[4:5], v[4:5], 0, v[206:207]
	v_lshl_add_u64 v[2:3], v[2:3], 0, v[206:207]
	s_waitcnt vmcnt(21)
; __device__ __forceinline__ float bflo(unsigned w) { return __uint_as_float(w << 16); }
; __device__ __forceinline__ float bfhi(unsigned w) { return __uint_as_float(w & 0xffff0000u); }
; __device__ __forceinline__ unsigned short f2bf(float f) { return (unsigned short)(cvt_pk_bf16(f, 0.f) & 0xffffu); }
; __device__ __forceinline__ void sgu_unit(const Params& p, int l, int un, LAS unsigned char* lds) {
;     ...
;     for (int qi = 0; qi < 16; ++qi) { const int q = wave * 16 + qi;
;         const u32x4 v = vv[qi]; float f[8] = {bflo(v.x), bfhi(v.x), bflo(v.y), bfhi(v.y), bflo(v.z), bfhi(v.z), bflo(v.w), bfhi(v.w)}; float ss = 0.f;
; #pragma unroll
;         for (int j = 0; j < 8; ++j) { f[j] = gelu_tanh(f[j]); ss += f[j] * f[j]; }
;         ss = wave_sum(ss); const float rinv = rsqrtf(ss * (1.0f / 512.0f) + EPS);
;         if ((lane >> 4) == h) { const int c0 = (lane & 15) * 8; const float* g = p.in[I_SGUNG] + l * 512 + h * 128 + c0;
; #pragma unroll
;             for (int j = 0; j < 8; ++j) Vl[(c0 + j) * 136 + q] = f2bf(f[j] * rinv * g[j]); } }
	v_cvt_pk_bf16_f32 v66, v66, v67
	v_cvt_pk_bf16_f32 v67, v68, v69
	v_mad_u64_u32 v[68:69], s[2:3], v63, s13, v[114:115]
	global_load_dwordx4 v[6:9], v[4:5], off offset:1024
	s_nop 0
	global_load_dwordx4 v[2:5], v[2:3], off offset:1024
	ds_write_b64 v68, v[66:67]
	v_ashrrev_i32_e32 v66, 7, v62
	s_waitcnt vmcnt(22)
	v_cvt_pk_bf16_f32 v62, v70, v71
	v_cvt_pk_bf16_f32 v63, v72, v73
	v_mad_u64_u32 v[66:67], s[2:3], v66, s13, v[114:115]
	ds_write_b64 v66, v[62:63]
	v_ashrrev_i32_e32 v66, 7, v102
	s_waitcnt vmcnt(21)
	v_cvt_pk_bf16_f32 v62, v74, v75
	v_cvt_pk_bf16_f32 v63, v76, v77
	v_mad_u64_u32 v[66:67], s[2:3], v66, s13, v[114:115]
	ds_write_b64 v66, v[62:63]
	v_ashrrev_i32_e32 v66, 7, v104
	s_waitcnt vmcnt(20)
	v_cvt_pk_bf16_f32 v62, v78, v79
	v_cvt_pk_bf16_f32 v63, v80, v81
	v_mad_u64_u32 v[66:67], s[2:3], v66, s13, v[114:115]
	ds_write_b64 v66, v[62:63]
	v_ashrrev_i32_e32 v66, 7, v106
	s_waitcnt vmcnt(19)
	v_cvt_pk_bf16_f32 v62, v82, v83
	v_cvt_pk_bf16_f32 v63, v84, v85
	v_mad_u64_u32 v[66:67], s[2:3], v66, s13, v[114:115]
	ds_write_b64 v66, v[62:63]
	v_ashrrev_i32_e32 v66, 7, v108
	s_waitcnt vmcnt(18)
	v_cvt_pk_bf16_f32 v62, v86, v87
	v_cvt_pk_bf16_f32 v63, v88, v89
	v_mad_u64_u32 v[66:67], s[2:3], v66, s13, v[114:115]
	ds_write_b64 v66, v[62:63]
	v_ashrrev_i32_e32 v66, 7, v110
	s_waitcnt vmcnt(17)
	v_cvt_pk_bf16_f32 v62, v90, v91
	v_cvt_pk_bf16_f32 v63, v92, v93
	v_mad_u64_u32 v[66:67], s[2:3], v66, s13, v[114:115]
	ds_write_b64 v66, v[62:63]
	v_ashrrev_i32_e32 v66, 7, v112
	v_mad_u64_u32 v[66:67], s[2:3], v66, s13, v[114:115]
	s_waitcnt vmcnt(15)
	v_and_b32_e32 v67, 0xffff0000, v98
	v_mul_f32_e32 v73, 0x3dd2d3e8, v67
	v_fma_f32 v73, -v73, v67, s33
	v_mul_f32_e32 v73, v73, v67
	v_exp_f32_e32 v73, v73
	v_cvt_pk_bf16_f32 v62, v94, v95
	v_cvt_pk_bf16_f32 v63, v96, v97
	ds_write_b64 v66, v[62:63]
	v_lshlrev_b32_e32 v66, 16, v98
	v_add_f32_e32 v73, 1.0, v73
	v_mul_f32_e32 v72, 0x3dd2d3e8, v66
	v_rcp_f32_e32 v73, v73
	v_fma_f32 v72, -v72, v66, s33
	v_mul_f32_e32 v72, v72, v66
	v_lshlrev_b32_e32 v69, 16, v99
	v_exp_f32_e32 v72, v72
	v_mul_f32_e32 v79, v73, v67
	v_mul_f32_e32 v67, 0x3dd2d3e8, v69
	v_fma_f32 v67, -v67, v69, s33
	v_mul_f32_e32 v67, v67, v69
	v_add_f32_e32 v72, 1.0, v72
	v_exp_f32_e32 v67, v67
	v_rcp_f32_e32 v72, v72
	v_lshlrev_b32_e32 v71, 16, v100
	v_and_b32_e32 v70, 0xffff0000, v99
	v_add_f32_e32 v67, 1.0, v67
	v_mul_f32_e32 v73, 0x3dd2d3e8, v71
	v_mul_f32_e32 v81, v72, v66
	v_mul_f32_e32 v72, 0x3dd2d3e8, v70
	v_rcp_f32_e32 v67, v67
	v_fma_f32 v73, -v73, v71, s33
	v_fma_f32 v72, -v72, v70, s33
	v_mul_f32_e32 v73, v73, v71
	v_mul_f32_e32 v72, v72, v70
	v_exp_f32_e32 v73, v73
	v_and_b32_e32 v74, 0xffff0000, v100
	v_exp_f32_e32 v72, v72
	v_mul_f32_e32 v80, v67, v69
	v_mul_f32_e32 v69, 0x3dd2d3e8, v74
	v_fma_f32 v69, -v69, v74, s33
	v_add_f32_e32 v67, 1.0, v73
	v_mul_f32_e32 v69, v69, v74
	v_add_f32_e32 v72, 1.0, v72
	v_rcp_f32_e32 v67, v67
	v_exp_f32_e32 v69, v69
	v_rcp_f32_e32 v72, v72
	v_lshlrev_b32_e32 v75, 16, v101
	v_and_b32_e32 v82, 0xffff0000, v101
	v_mul_f32_e32 v76, v67, v71
	v_add_f32_e32 v67, 1.0, v69
	v_mul_f32_e32 v69, 0x3dd2d3e8, v75
	v_mul_f32_e32 v78, v72, v70
	v_fma_f32 v69, -v69, v75, s33
	v_mul_f32_e32 v70, 0x3dd2d3e8, v82
	v_mul_f32_e32 v69, v69, v75
	v_fma_f32 v70, -v70, v82, s33
	v_rcp_f32_e32 v67, v67
	v_exp_f32_e32 v69, v69
	v_mul_f32_e32 v70, v70, v82
	v_exp_f32_e32 v70, v70
	v_mul_f32_e32 v66, v79, v79
	v_mul_f32_e32 v77, v67, v74
	v_add_f32_e32 v67, 1.0, v69
	v_fmac_f32_e32 v66, v81, v81
	v_rcp_f32_e32 v67, v67
	v_add_f32_e32 v69, 1.0, v70
	v_fmac_f32_e32 v66, v80, v80
	v_rcp_f32_e32 v69, v69
	v_and_b32_e32 v62, 64, v249
	v_fmac_f32_e32 v66, v78, v78
	v_add_u32_e32 v62, 64, v62
	v_xor_b32_e32 v63, 32, v249
	v_fmac_f32_e32 v66, v76, v76
	v_cmp_lt_i32_e32 vcc, v63, v62
	v_fmac_f32_e32 v66, v77, v77
	v_mul_f32_e32 v75, v67, v75
	v_cndmask_b32_e32 v63, v249, v63, vcc
	v_fmac_f32_e32 v66, v75, v75
	v_mul_f32_e32 v74, v69, v82
	v_lshlrev_b32_e32 v68, 2, v63
	v_fmac_f32_e32 v66, v74, v74
	v_mov_b32_e32 v67, v66
	s_nop 1
	v_permlane32_swap_b32_e32 v67, v66
	v_and_b32_e32 v84, 0x78, v105
	v_readlane_b32 s2, v253, 40
	s_waitcnt lgkmcnt(0)
	v_add_f32_e32 v66, v66, v67
	v_mov_b32_e32 v67, v66
	s_nop 1
	v_permlane16_swap_b32_e32 v67, v66
	v_lshlrev_b32_e32 v206, 2, v84
	v_readlane_b32 s45, v251, 17
	s_waitcnt lgkmcnt(0)
	v_add_f32_e32 v66, v66, v67
	s_nop 1
	v_mov_b32_dpp v67, v66 row_ror:8 row_mask:0xf bank_mask:0xf
	v_readlane_b32 s46, v251, 18
	v_readlane_b32 s47, v251, 19
	s_waitcnt lgkmcnt(0)
	v_add_f32_e32 v66, v66, v67
	s_nop 1
	v_mov_b32_dpp v67, v66 row_shl:4 row_mask:0xf bank_mask:0x5
	v_mov_b32_dpp v67, v66 row_shr:4 row_mask:0xf bank_mask:0xa
	v_readlane_b32 s56, v251, 28
	v_readlane_b32 s57, v251, 29
	v_readlane_b32 s58, v251, 30
	v_readlane_b32 s59, v251, 31
	s_waitcnt lgkmcnt(0)
	v_add_f32_e32 v63, v66, v67
	s_nop 1
	v_mov_b32_dpp v67, v63 quad_perm:[2,3,0,1] row_mask:0xf bank_mask:0xf
	v_bfe_u32 v66, v64, 4, 2
	v_cmp_eq_u32_e32 vcc, s2, v66
	s_mov_b64 s[16:17], s[52:53]
	s_waitcnt lgkmcnt(0)
	v_add_f32_e32 v82, v63, v67
	s_nop 1
	v_mov_b32_dpp v83, v82 quad_perm:[1,0,3,2] row_mask:0xf bank_mask:0xf
	v_lshl_add_u32 v67, v103, 5, 0
	v_lshl_add_u64 v[62:63], s[0:1], 0, v[206:207]
	v_mad_u32_u24 v67, v84, s13, v67
	v_lshrrev_b32_e32 v170, 6, v0
	v_lshlrev_b32_e32 v170, 1, v170
	v_and_b32_e32 v171, 15, v0
	v_xor_b32_e32 v168, v170, v171
	v_sub_u32_e32 v168, v168, v170
	v_lshl_add_u32 v168, v168, 4, v67
	v_or_b32_e32 v170, 1, v170
	v_xor_b32_e32 v169, v170, v171
	v_sub_u32_e32 v169, v169, v170
	v_lshl_add_u32 v169, v169, 4, v67
	s_mov_b64 s[18:19], s[54:55]
	s_and_saveexec_b64 s[0:1], vcc
	s_cbranch_execz .LBB0_1262
; __device__ __forceinline__ unsigned short f2bf(float f) { return (unsigned short)(cvt_pk_bf16(f, 0.f) & 0xffffu); }
; __device__ __forceinline__ void sgu_unit(const Params& p, int l, int un, LAS unsigned char* lds) {
;     ...
;         ss = wave_sum(ss); const float rinv = rsqrtf(ss * (1.0f / 512.0f) + EPS);
;         if ((lane >> 4) == h) { const int c0 = (lane & 15) * 8; const float* g = p.in[I_SGUNG] + l * 512 + h * 128 + c0;
; #pragma unroll
;             for (int j = 0; j < 8; ++j) Vl[(c0 + j) * 136 + q] = f2bf(f[j] * rinv * g[j]); } }
	s_waitcnt lgkmcnt(0)
	v_add_f32_e32 v82, v82, v83
	v_fmamk_f32 v82, v82, 0x3b000000, v246
	s_mov_b32 s2, 0x800000
	v_cmp_gt_f32_e64 s[2:3], s2, v82
	v_mul_f32_e32 v83, 0x4b800000, v82
	s_nop 0
	v_cndmask_b32_e64 v82, v82, v83, s[2:3]
	v_rsq_f32_e32 v82, v82
	s_nop 0
	v_mul_f32_e32 v83, 0x45800000, v82
	v_cndmask_b32_e64 v90, v82, v83, s[2:3]
	global_load_dwordx4 v[82:85], v[62:63], off offset:16
	global_load_dwordx4 v[86:89], v[62:63], off
	v_mul_f32_e32 v79, v79, v90
	v_mul_f32_e32 v76, v76, v90
	v_mul_f32_e32 v81, v81, v90
	v_mul_f32_e32 v78, v78, v90
	v_mul_f32_e32 v75, v75, v90
	v_mul_f32_e32 v74, v74, v90
	s_waitcnt vmcnt(1)
	v_mul_f32_e32 v76, v76, v82
	s_waitcnt vmcnt(0)
	v_mov_b32_e32 v160, v86
	v_mov_b32_e32 v161, v87
	v_mov_b32_e32 v162, v88
	v_mov_b32_e32 v163, v89
	v_mov_b32_e32 v164, v82
	v_mov_b32_e32 v165, v83
	v_mov_b32_e32 v166, v84
	v_mov_b32_e32 v167, v85
	v_mul_f32_e32 v79, v79, v87
	v_cvt_pk_bf16_f32 v79, v79, s0
	v_cvt_pk_bf16_f32 v76, v76, s0
	ds_write_b16 v168, v79 offset:35088
	v_mul_f32_e32 v79, v80, v90
	ds_write_b16 v168, v76 offset:35904
	v_mul_f32_e32 v76, v77, v90
	v_mul_f32_e32 v81, v81, v86
	v_mul_f32_e32 v79, v79, v88
	v_mul_f32_e32 v78, v78, v89
	v_mul_f32_e32 v76, v76, v83
	v_mul_f32_e32 v75, v75, v84
	v_mul_f32_e32 v74, v74, v85
	v_cvt_pk_bf16_f32 v81, v81, s0
	v_cvt_pk_bf16_f32 v79, v79, s0
	v_cvt_pk_bf16_f32 v78, v78, s0
	v_cvt_pk_bf16_f32 v76, v76, s0
	v_cvt_pk_bf16_f32 v75, v75, s0
	v_cvt_pk_bf16_f32 v74, v74, s0
	ds_write_b16 v168, v81 offset:34816
	ds_write_b16 v168, v79 offset:35360
	ds_write_b16 v168, v78 offset:35632
	ds_write_b16 v168, v76 offset:36176
	ds_write_b16 v168, v75 offset:36448
	ds_write_b16 v168, v74 offset:36720

; #define LAS __attribute__((address_space(3)))
; __device__ __forceinline__ int opaque_tid() { int t = threadIdx.x; asm volatile("" : "+v"(t)); return t; }
; __device__ __forceinline__ unsigned char* opaque_ptr(unsigned char* q) { long z = 0; asm volatile("" : "+s"(z)); return q + z; }
; __device__ __forceinline__ void sgu_unit(const Params& p, int l, int un, LAS unsigned char* lds) {
;     const int tid = opaque_tid(), lane = tid & 63, wave = tid >> 6;
;     unsigned char* ws = opaque_ptr(p.ws);
;     const bf16_t* P = (const bf16_t*)(ws + WS_PA);
;     bf16_t* CAT = (bf16_t*)(ws + WS_CAT);
;     const int cc = un >> 2, h = un & 3; const int row0 = cc * 128;
;     LAS bf16_t* Wl = (LAS bf16_t*)lds;
;     LAS bf16_t* Vl = (LAS bf16_t*)(lds + 128 * 136 * 2);
;     const float* Wg = p.in[I_SGUW] + ((size_t)l * 4 + h) * 128 * 128;
;     f32x4 wq[8]; u32x4 vv[16];
; #pragma unroll
;     for (int i = 0; i < 8; ++i) wq[i] = *(const f32x4*)(Wg + (i * 512 + tid) * 4);
; #pragma unroll
;     for (int qi = 0; qi < 16; ++qi) vv[qi] = *(const u32x4*)(P + (size_t)(row0 + wave * 16 + qi) * INP + C_SGU_V + lane * 8);
; __global__ void __launch_bounds__(512, 2) fwd(Params p) {
;     ...
;             if (c < (l == 0 ? 72 : 64) || G != 256) pg8::gemm_phase(lds, pg8::Desc{512, 512, 512}, S, E);
;             else { const int un = (l == 0 ? 128 + (c - 72) : 160 + (c - 64)); if (un < (l == 0 ? B_SGU : 256)) sgu_unit(p, l, un, lds); }
.LBB0_1393:
	s_andn2_b64 vcc, exec, s[0:1]
	s_cbranch_vccnz .LBB0_1501
	v_readlane_b32 s0, v252, 5
	v_readlane_b32 s1, v252, 6
	s_lshl_b32 s4, s0, 9
	v_readlane_b32 s0, v252, 20
	v_readlane_b32 s1, v252, 21
	s_and_b64 s[0:1], s[0:1], exec
	s_cselect_b32 s0, 0x48, 64
	s_cmp_ge_i32 s92, s0
	v_readlane_b32 s12, v255, 40
	s_cselect_b64 s[2:3], -1, 0
	v_readlane_b32 s13, v255, 41
	s_and_b64 s[2:3], s[12:13], s[2:3]
	s_mov_b64 s[0:1], -1
	s_and_b64 vcc, exec, s[2:3]
	s_cbranch_vccz .LBB0_1430
	v_readlane_b32 s2, v252, 20
	v_readlane_b32 s3, v252, 21
	s_and_b64 s[0:1], s[2:3], exec
	s_cselect_b32 s0, 56, 0x60
	s_add_i32 s0, s0, s92
	s_and_b64 s[2:3], s[2:3], exec
	s_movk_i32 s1, 0x120
	s_cselect_b32 s1, s1, 0x100
	s_cmp_ge_u32 s0, s1
	s_cbranch_scc1 .LBB0_1429
	v_readlane_b32 s44, v251, 16
	s_lshl_b32 s12, s0, 5
	v_readlane_b32 s0, v253, 39
	v_readlane_b32 s48, v251, 20
	v_readlane_b32 s49, v251, 21
	s_or_b32 s40, s4, s0
	s_mov_b32 s41, s5
	v_readlane_b32 s50, v251, 22
	v_readlane_b32 s51, v251, 23
	v_readlane_b32 s52, v251, 24
	v_readlane_b32 s53, v251, 25
	v_readlane_b32 s54, v251, 26
	v_readlane_b32 s55, v251, 27
	s_mov_b64 s[16:17], s[48:49]
	s_lshl_b64 s[0:1], s[40:41], 9
	s_mov_b64 s[18:19], s[50:51]
	s_waitcnt vmcnt(0)
	v_mov_b32_e32 v64, v0
	s_add_u32 s2, s18, s0
	s_addc_u32 s3, s19, s1
	v_lshlrev_b32_e32 v2, 2, v64
	v_ashrrev_i32_e32 v3, 31, v2
	v_add_u32_e32 v62, 0x800, v2
	s_mov_b64 s[14:15], 0
	v_lshl_add_u64 v[4:5], v[2:3], 2, s[2:3]
	v_ashrrev_i32_e32 v63, 31, v62
	v_lshl_add_u64 v[6:7], v[62:63], 2, s[2:3]
	global_load_dwordx4 v[66:69], v[4:5], off
	global_load_dwordx4 v[70:73], v[6:7], off
	v_add_u32_e32 v102, 0x1000, v2
	v_ashrrev_i32_e32 v103, 31, v102
	v_add_u32_e32 v104, 0x1800, v2
	v_lshl_add_u64 v[4:5], v[102:103], 2, s[2:3]
	v_ashrrev_i32_e32 v105, 31, v104
	v_lshl_add_u64 v[6:7], v[104:105], 2, s[2:3]
	global_load_dwordx4 v[74:77], v[4:5], off
	global_load_dwordx4 v[78:81], v[6:7], off
	s_and_b32 s12, s12, 0x7fffff80
	s_lshl_b64 s[0:1], s[4:5], 2
	v_readlane_b32 s13, v253, 41
	v_add_u32_e32 v106, 0x2000, v2
	s_add_u32 s0, s13, s0
	v_readlane_b32 s13, v253, 42
	v_ashrrev_i32_e32 v107, 31, v106
	v_add_u32_e32 v108, 0x2800, v2
	s_addc_u32 s1, s13, s1
	v_lshl_add_u64 v[4:5], v[106:107], 2, s[2:3]
	v_ashrrev_i32_e32 v109, 31, v108
	s_add_u32 s36, s84, s14
	v_lshl_add_u64 v[6:7], v[108:109], 2, s[2:3]
	global_load_dwordx4 v[82:85], v[4:5], off
	global_load_dwordx4 v[86:89], v[6:7], off
	s_addc_u32 s37, s85, s15
	v_add_u32_e32 v110, 0x3000, v2
	v_add_u32_e32 v112, 0x3800, v2
	s_add_u32 s38, s36, 0x1f1b8000
	v_ashrrev_i32_e32 v111, 31, v110
	v_ashrrev_i32_e32 v113, 31, v112
	v_ashrrev_i32_e32 v103, 6, v64
	s_addc_u32 s39, s37, 0
	v_lshl_add_u64 v[4:5], v[110:111], 2, s[2:3]
	v_lshl_add_u64 v[2:3], v[112:113], 2, s[2:3]
	v_lshlrev_b32_e32 v65, 4, v103
	v_and_b32_e32 v8, 63, v64
	global_load_dwordx4 v[90:93], v[4:5], off
	global_load_dwordx4 v[94:97], v[2:3], off
	v_add_u32_e32 v9, s12, v65
	v_mov_b64_e32 v[2:3], s[38:39]
	s_movk_i32 s13, 0x1e00
	v_mad_i64_i32 v[4:5], s[2:3], v9, s13, v[2:3]
	v_lshlrev_b32_e32 v206, 4, v8
	v_or_b32_e32 v6, 1, v9
	v_lshl_add_u64 v[4:5], v[4:5], 0, v[206:207]
	v_mad_i64_i32 v[6:7], s[2:3], v6, s13, v[2:3]
	v_lshl_add_u64 v[6:7], v[6:7], 0, v[206:207]
	global_load_dwordx4 v[98:101], v[4:5], off offset:1024
	global_load_dwordx4 v[58:61], v[6:7], off offset:1024
	v_or_b32_e32 v4, 2, v9
	v_or_b32_e32 v6, 3, v9
	v_mad_i64_i32 v[4:5], s[2:3], v4, s13, v[2:3]
	v_mad_i64_i32 v[6:7], s[2:3], v6, s13, v[2:3]
	v_lshl_add_u64 v[4:5], v[4:5], 0, v[206:207]
	v_lshl_add_u64 v[6:7], v[6:7], 0, v[206:207]
	global_load_dwordx4 v[54:57], v[4:5], off offset:1024
	global_load_dwordx4 v[50:53], v[6:7], off offset:1024
	v_or_b32_e32 v4, 4, v9
	v_or_b32_e32 v6, 5, v9
	v_mad_i64_i32 v[4:5], s[2:3], v4, s13, v[2:3]
	v_mad_i64_i32 v[6:7], s[2:3], v6, s13, v[2:3]
	v_lshl_add_u64 v[4:5], v[4:5], 0, v[206:207]
	v_lshl_add_u64 v[6:7], v[6:7], 0, v[206:207]
	global_load_dwordx4 v[46:49], v[4:5], off offset:1024
	global_load_dwordx4 v[42:45], v[6:7], off offset:1024
	v_or_b32_e32 v4, 6, v9
	v_or_b32_e32 v6, 7, v9
	v_mad_i64_i32 v[4:5], s[2:3], v4, s13, v[2:3]
	v_mad_i64_i32 v[6:7], s[2:3], v6, s13, v[2:3]
	v_lshl_add_u64 v[4:5], v[4:5], 0, v[206:207]
	v_lshl_add_u64 v[6:7], v[6:7], 0, v[206:207]
	global_load_dwordx4 v[38:41], v[4:5], off offset:1024
	global_load_dwordx4 v[34:37], v[6:7], off offset:1024
	v_or_b32_e32 v4, 8, v9
	v_or_b32_e32 v6, 9, v9
	v_mad_i64_i32 v[4:5], s[2:3], v4, s13, v[2:3]
	v_mad_i64_i32 v[6:7], s[2:3], v6, s13, v[2:3]
	v_lshl_add_u64 v[4:5], v[4:5], 0, v[206:207]
	v_lshl_add_u64 v[6:7], v[6:7], 0, v[206:207]
	global_load_dwordx4 v[30:33], v[4:5], off offset:1024
	global_load_dwordx4 v[26:29], v[6:7], off offset:1024
	v_or_b32_e32 v4, 10, v9
	v_or_b32_e32 v6, 11, v9
	v_mad_i64_i32 v[4:5], s[2:3], v4, s13, v[2:3]
	v_mad_i64_i32 v[6:7], s[2:3], v6, s13, v[2:3]
	v_lshl_add_u64 v[4:5], v[4:5], 0, v[206:207]
	v_lshl_add_u64 v[6:7], v[6:7], 0, v[206:207]
	global_load_dwordx4 v[22:25], v[4:5], off offset:1024
	global_load_dwordx4 v[18:21], v[6:7], off offset:1024
	v_or_b32_e32 v4, 12, v9
	v_or_b32_e32 v6, 13, v9
	v_mad_i64_i32 v[4:5], s[2:3], v4, s13, v[2:3]
	v_mad_i64_i32 v[6:7], s[2:3], v6, s13, v[2:3]
	v_lshl_add_u64 v[4:5], v[4:5], 0, v[206:207]
	v_lshl_add_u64 v[6:7], v[6:7], 0, v[206:207]
	v_lshlrev_b32_e32 v105, 3, v64
	global_load_dwordx4 v[14:17], v[4:5], off offset:1024
	global_load_dwordx4 v[10:13], v[6:7], off offset:1024
	v_or_b32_e32 v4, 14, v9
	v_or_b32_e32 v6, 15, v9
	v_and_b32_e32 v63, 0xf8, v105
	v_mad_i64_i32 v[4:5], s[2:3], v4, s13, v[2:3]
	v_mad_i64_i32 v[2:3], s[2:3], v6, s13, v[2:3]
	v_add_u32_e32 v114, 0, v63
	v_bfe_i32 v63, v64, 5, 25
	s_movk_i32 s13, 0x110
	v_lshl_add_u64 v[4:5], v[4:5], 0, v[206:207]
	v_lshl_add_u64 v[2:3], v[2:3], 0, v[206:207]
	s_waitcnt vmcnt(21)
; __device__ __forceinline__ float bflo(unsigned w) { return __uint_as_float(w << 16); }
; __device__ __forceinline__ float bfhi(unsigned w) { return __uint_as_float(w & 0xffff0000u); }
; __device__ __forceinline__ unsigned short f2bf(float f) { return (unsigned short)(cvt_pk_bf16(f, 0.f) & 0xffffu); }
; __device__ __forceinline__ void sgu_unit(const Params& p, int l, int un, LAS unsigned char* lds) {
;     ...
;     for (int qi = 0; qi < 16; ++qi) { const int q = wave * 16 + qi;
;         const u32x4 v = vv[qi]; float f[8] = {bflo(v.x), bfhi(v.x), bflo(v.y), bfhi(v.y), bflo(v.z), bfhi(v.z), bflo(v.w), bfhi(v.w)}; float ss = 0.f;
; #pragma unroll
;         for (int j = 0; j < 8; ++j) { f[j] = gelu_tanh(f[j]); ss += f[j] * f[j]; }
;         ss = wave_sum(ss); const float rinv = rsqrtf(ss * (1.0f / 512.0f) + EPS);
;         if ((lane >> 4) == h) { const int c0 = (lane & 15) * 8; const float* g = p.in[I_SGUNG] + l * 512 + h * 128 + c0;
; #pragma unroll
;             for (int j = 0; j < 8; ++j) Vl[(c0 + j) * 136 + q] = f2bf(f[j] * rinv * g[j]); } }
	v_cvt_pk_bf16_f32 v66, v66, v67
	v_cvt_pk_bf16_f32 v67, v68, v69
	v_mad_u64_u32 v[68:69], s[2:3], v63, s13, v[114:115]
	global_load_dwordx4 v[6:9], v[4:5], off offset:1024
	s_nop 0
	global_load_dwordx4 v[2:5], v[2:3], off offset:1024
	ds_write_b64 v68, v[66:67]
	v_ashrrev_i32_e32 v66, 7, v62
	s_waitcnt vmcnt(22)
	v_cvt_pk_bf16_f32 v62, v70, v71
	v_cvt_pk_bf16_f32 v63, v72, v73
	v_mad_u64_u32 v[66:67], s[2:3], v66, s13, v[114:115]
	ds_write_b64 v66, v[62:63]
	v_ashrrev_i32_e32 v66, 7, v102
	s_waitcnt vmcnt(21)
	v_cvt_pk_bf16_f32 v62, v74, v75
	v_cvt_pk_bf16_f32 v63, v76, v77
	v_mad_u64_u32 v[66:67], s[2:3], v66, s13, v[114:115]
	ds_write_b64 v66, v[62:63]
	v_ashrrev_i32_e32 v66, 7, v104
	s_waitcnt vmcnt(20)
	v_cvt_pk_bf16_f32 v62, v78, v79
	v_cvt_pk_bf16_f32 v63, v80, v81
	v_mad_u64_u32 v[66:67], s[2:3], v66, s13, v[114:115]
	ds_write_b64 v66, v[62:63]
	v_ashrrev_i32_e32 v66, 7, v106
	s_waitcnt vmcnt(19)
	v_cvt_pk_bf16_f32 v62, v82, v83
	v_cvt_pk_bf16_f32 v63, v84, v85
	v_mad_u64_u32 v[66:67], s[2:3], v66, s13, v[114:115]
	ds_write_b64 v66, v[62:63]
	v_ashrrev_i32_e32 v66, 7, v108
	s_waitcnt vmcnt(18)
	v_cvt_pk_bf16_f32 v62, v86, v87
	v_cvt_pk_bf16_f32 v63, v88, v89
	v_mad_u64_u32 v[66:67], s[2:3], v66, s13, v[114:115]
	ds_write_b64 v66, v[62:63]
	v_ashrrev_i32_e32 v66, 7, v110
	s_waitcnt vmcnt(17)
	v_cvt_pk_bf16_f32 v62, v90, v91
	v_cvt_pk_bf16_f32 v63, v92, v93
	v_mad_u64_u32 v[66:67], s[2:3], v66, s13, v[114:115]
	ds_write_b64 v66, v[62:63]
	v_ashrrev_i32_e32 v66, 7, v112
	v_mad_u64_u32 v[66:67], s[2:3], v66, s13, v[114:115]
	s_waitcnt vmcnt(15)
	v_and_b32_e32 v67, 0xffff0000, v98
	v_mul_f32_e32 v73, 0x3dd2d3e8, v67
	v_fma_f32 v73, -v73, v67, s33
	v_mul_f32_e32 v73, v73, v67
	v_exp_f32_e32 v73, v73
	v_cvt_pk_bf16_f32 v62, v94, v95
	v_cvt_pk_bf16_f32 v63, v96, v97
	ds_write_b64 v66, v[62:63]
	v_lshlrev_b32_e32 v66, 16, v98
	v_add_f32_e32 v73, 1.0, v73
	v_mul_f32_e32 v72, 0x3dd2d3e8, v66
	v_rcp_f32_e32 v73, v73
	v_fma_f32 v72, -v72, v66, s33
	v_mul_f32_e32 v72, v72, v66
	v_lshlrev_b32_e32 v69, 16, v99
	v_exp_f32_e32 v72, v72
	v_mul_f32_e32 v79, v73, v67
	v_mul_f32_e32 v67, 0x3dd2d3e8, v69
	v_fma_f32 v67, -v67, v69, s33
	v_mul_f32_e32 v67, v67, v69
	v_add_f32_e32 v72, 1.0, v72
	v_exp_f32_e32 v67, v67
	v_rcp_f32_e32 v72, v72
	v_lshlrev_b32_e32 v71, 16, v100
	v_and_b32_e32 v70, 0xffff0000, v99
	v_add_f32_e32 v67, 1.0, v67
	v_mul_f32_e32 v73, 0x3dd2d3e8, v71
	v_mul_f32_e32 v81, v72, v66
	v_mul_f32_e32 v72, 0x3dd2d3e8, v70
	v_rcp_f32_e32 v67, v67
	v_fma_f32 v73, -v73, v71, s33
	v_fma_f32 v72, -v72, v70, s33
	v_mul_f32_e32 v73, v73, v71
	v_mul_f32_e32 v72, v72, v70
	v_exp_f32_e32 v73, v73
	v_and_b32_e32 v74, 0xffff0000, v100
	v_exp_f32_e32 v72, v72
	v_mul_f32_e32 v80, v67, v69
	v_mul_f32_e32 v69, 0x3dd2d3e8, v74
	v_fma_f32 v69, -v69, v74, s33
	v_add_f32_e32 v67, 1.0, v73
	v_mul_f32_e32 v69, v69, v74
	v_add_f32_e32 v72, 1.0, v72
	v_rcp_f32_e32 v67, v67
	v_exp_f32_e32 v69, v69
	v_rcp_f32_e32 v72, v72
	v_lshlrev_b32_e32 v75, 16, v101
	v_and_b32_e32 v82, 0xffff0000, v101
	v_mul_f32_e32 v76, v67, v71
	v_add_f32_e32 v67, 1.0, v69
	v_mul_f32_e32 v69, 0x3dd2d3e8, v75
	v_mul_f32_e32 v78, v72, v70
	v_fma_f32 v69, -v69, v75, s33
	v_mul_f32_e32 v70, 0x3dd2d3e8, v82
	v_mul_f32_e32 v69, v69, v75
	v_fma_f32 v70, -v70, v82, s33
	v_rcp_f32_e32 v67, v67
	v_exp_f32_e32 v69, v69
	v_mul_f32_e32 v70, v70, v82
	v_exp_f32_e32 v70, v70
	v_mul_f32_e32 v66, v79, v79
	v_mul_f32_e32 v77, v67, v74
	v_add_f32_e32 v67, 1.0, v69
	v_fmac_f32_e32 v66, v81, v81
	v_rcp_f32_e32 v67, v67
	v_add_f32_e32 v69, 1.0, v70
	v_fmac_f32_e32 v66, v80, v80
	v_rcp_f32_e32 v69, v69
	v_and_b32_e32 v62, 64, v249
	v_fmac_f32_e32 v66, v78, v78
	v_add_u32_e32 v62, 64, v62
	v_xor_b32_e32 v63, 32, v249
	v_fmac_f32_e32 v66, v76, v76
	v_cmp_lt_i32_e32 vcc, v63, v62
	v_fmac_f32_e32 v66, v77, v77
	v_mul_f32_e32 v75, v67, v75
	v_cndmask_b32_e32 v63, v249, v63, vcc
	v_fmac_f32_e32 v66, v75, v75
	v_mul_f32_e32 v74, v69, v82
	v_lshlrev_b32_e32 v68, 2, v63
	v_fmac_f32_e32 v66, v74, v74
	v_mov_b32_e32 v67, v66
	s_nop 1
	v_permlane32_swap_b32_e32 v67, v66
	v_and_b32_e32 v84, 0x78, v105
	v_readlane_b32 s2, v253, 40
	s_waitcnt lgkmcnt(0)
	v_add_f32_e32 v66, v66, v67
	v_mov_b32_e32 v67, v66
	s_nop 1
	v_permlane16_swap_b32_e32 v67, v66
	v_lshlrev_b32_e32 v206, 2, v84
	v_readlane_b32 s45, v251, 17
	s_waitcnt lgkmcnt(0)
	v_add_f32_e32 v66, v66, v67
	s_nop 1
	v_mov_b32_dpp v67, v66 row_ror:8 row_mask:0xf bank_mask:0xf
	v_readlane_b32 s46, v251, 18
	v_readlane_b32 s47, v251, 19
	s_waitcnt lgkmcnt(0)
	v_add_f32_e32 v66, v66, v67
	s_nop 1
	v_mov_b32_dpp v67, v66 row_shl:4 row_mask:0xf bank_mask:0x5
	v_mov_b32_dpp v67, v66 row_shr:4 row_mask:0xf bank_mask:0xa
	v_readlane_b32 s56, v251, 28
	v_readlane_b32 s57, v251, 29
	v_readlane_b32 s58, v251, 30
	v_readlane_b32 s59, v251, 31
	s_waitcnt lgkmcnt(0)
	v_add_f32_e32 v63, v66, v67
	s_nop 1
	v_mov_b32_dpp v67, v63 quad_perm:[2,3,0,1] row_mask:0xf bank_mask:0xf
	v_bfe_u32 v66, v64, 4, 2
	v_cmp_eq_u32_e32 vcc, s2, v66
	s_mov_b64 s[20:21], s[52:53]
	s_waitcnt lgkmcnt(0)
	v_add_f32_e32 v82, v63, v67
	s_nop 1
	v_mov_b32_dpp v83, v82 quad_perm:[1,0,3,2] row_mask:0xf bank_mask:0xf
	v_lshl_add_u32 v67, v103, 5, 0
	v_lshl_add_u64 v[62:63], s[0:1], 0, v[206:207]
	v_mad_u32_u24 v67, v84, s13, v67
	v_lshrrev_b32_e32 v170, 6, v0
	v_lshlrev_b32_e32 v170, 1, v170
	v_and_b32_e32 v171, 15, v0
	v_xor_b32_e32 v168, v170, v171
	v_sub_u32_e32 v168, v168, v170
	v_lshl_add_u32 v168, v168, 4, v67
	v_or_b32_e32 v170, 1, v170
	v_xor_b32_e32 v169, v170, v171
	v_sub_u32_e32 v169, v169, v170
	v_lshl_add_u32 v169, v169, 4, v67
	s_mov_b64 s[22:23], s[54:55]
	s_and_saveexec_b64 s[0:1], vcc
	s_cbranch_execz .LBB0_1398
; __device__ __forceinline__ unsigned short f2bf(float f) { return (unsigned short)(cvt_pk_bf16(f, 0.f) & 0xffffu); }
; __device__ __forceinline__ void sgu_unit(const Params& p, int l, int un, LAS unsigned char* lds) {
;     ...
;         ss = wave_sum(ss); const float rinv = rsqrtf(ss * (1.0f / 512.0f) + EPS);
;         if ((lane >> 4) == h) { const int c0 = (lane & 15) * 8; const float* g = p.in[I_SGUNG] + l * 512 + h * 128 + c0;
; #pragma unroll
;             for (int j = 0; j < 8; ++j) Vl[(c0 + j) * 136 + q] = f2bf(f[j] * rinv * g[j]); } }
	s_waitcnt lgkmcnt(0)
	v_add_f32_e32 v82, v82, v83
	v_fmamk_f32 v82, v82, 0x3b000000, v246
	s_mov_b32 s2, 0x800000
	v_cmp_gt_f32_e64 s[2:3], s2, v82
	v_mul_f32_e32 v83, 0x4b800000, v82
	s_nop 0
	v_cndmask_b32_e64 v82, v82, v83, s[2:3]
	v_rsq_f32_e32 v82, v82
	s_nop 0
	v_mul_f32_e32 v83, 0x45800000, v82
	v_cndmask_b32_e64 v90, v82, v83, s[2:3]
	global_load_dwordx4 v[82:85], v[62:63], off offset:16
	global_load_dwordx4 v[86:89], v[62:63], off
	v_mul_f32_e32 v79, v79, v90
	v_mul_f32_e32 v76, v76, v90
	v_mul_f32_e32 v81, v81, v90
	v_mul_f32_e32 v78, v78, v90
	v_mul_f32_e32 v75, v75, v90
	v_mul_f32_e32 v74, v74, v90
	s_waitcnt vmcnt(1)
	v_mul_f32_e32 v76, v76, v82
	s_waitcnt vmcnt(0)
	v_mov_b32_e32 v160, v86
	v_mov_b32_e32 v161, v87
	v_mov_b32_e32 v162, v88
	v_mov_b32_e32 v163, v89
	v_mov_b32_e32 v164, v82
	v_mov_b32_e32 v165, v83
	v_mov_b32_e32 v166, v84
	v_mov_b32_e32 v167, v85
	v_mul_f32_e32 v79, v79, v87
	v_cvt_pk_bf16_f32 v79, v79, s0
	v_cvt_pk_bf16_f32 v76, v76, s0
	ds_write_b16 v168, v79 offset:35088
	v_mul_f32_e32 v79, v80, v90
	ds_write_b16 v168, v76 offset:35904
	v_mul_f32_e32 v76, v77, v90
	v_mul_f32_e32 v81, v81, v86
	v_mul_f32_e32 v79, v79, v88
	v_mul_f32_e32 v78, v78, v89
	v_mul_f32_e32 v76, v76, v83
	v_mul_f32_e32 v75, v75, v84
	v_mul_f32_e32 v74, v74, v85
	v_cvt_pk_bf16_f32 v81, v81, s0
	v_cvt_pk_bf16_f32 v79, v79, s0
	v_cvt_pk_bf16_f32 v78, v78, s0
	v_cvt_pk_bf16_f32 v76, v76, s0
	v_cvt_pk_bf16_f32 v75, v75, s0
	v_cvt_pk_bf16_f32 v74, v74, s0
	ds_write_b16 v168, v81 offset:34816
	ds_write_b16 v168, v79 offset:35360
	ds_write_b16 v168, v78 offset:35632
	ds_write_b16 v168, v76 offset:36176
	ds_write_b16 v168, v75 offset:36448
	ds_write_b16 v168, v74 offset:36720
